# norm1 rows: expert-combine turn takes up to four experts, second pair's row gathers issued before the first pair's math
# baseline (speedup 1.0000x reference)
.LBB0_157:
	s_add_u32 s50, s46, -1
	s_addc_u32 s51, s47, -1
	s_and_b64 vcc, s[50:51], s[46:47]
	s_mulk_i32 s43, 0x900
	s_ashr_i32 s47, s48, 31
	s_add_u32 s46, s48, s43
	s_addc_u32 s47, s47, 0
	s_mulk_i32 s7, 0x900
	s_ashr_i32 s43, s1, 31
	v_lshl_add_u64 v[176:177], s[46:47], 0, v[160:161]
	s_add_u32 s46, s7, s1
	s_addc_u32 s47, 0, s43
	v_lshl_add_u64 v[184:185], s[46:47], 0, v[160:161]
	v_lshlrev_b64 v[176:177], 11, v[176:177]
	v_lshlrev_b64 v[184:185], 11, v[184:185]
	v_lshl_add_u64 v[176:177], v[138:139], 0, v[176:177]
	v_lshl_add_u64 v[184:185], v[138:139], 0, v[184:185]
	global_load_dwordx2 v[178:179], v[176:177], off nt
	global_load_dwordx2 v[180:181], v[176:177], off offset:512 nt
	global_load_dwordx2 v[182:183], v[176:177], off offset:1024 nt
	global_load_dwordx2 v[176:177], v[176:177], off offset:1536 nt
	s_nop 0
	global_load_dwordx2 v[186:187], v[184:185], off nt
	global_load_dwordx2 v[188:189], v[184:185], off offset:512 nt
	global_load_dwordx2 v[190:191], v[184:185], off offset:1024 nt
	s_nop 0
	global_load_dwordx2 v[184:185], v[184:185], off offset:1536 nt
	s_cmp_eq_u64 vcc, 0
	s_cbranch_scc1 .Lcmb_noB
	s_add_u32 s50, vcc_lo, -1
	s_addc_u32 s51, vcc_hi, -1
	s_and_b64 s[46:47], s[50:51], vcc
	s_cmp_eq_u64 s[46:47], 0
	s_cselect_b64 s[50:51], -1, 0
	s_ff1_i32_b64 s43, vcc
	s_ff1_i32_b64 s49, s[46:47]
	s_and_b64 s[50:51], s[50:51], exec
	s_cselect_b32 s7, s43, s49
	v_readlane_b32 s48, v170, s43
	v_readlane_b32 s1, v170, s7
	v_readlane_b32 s100, v171, s43
	s_mov_b32 s101, 0
	s_cbranch_scc1 .Lcmb_b1
	v_readlane_b32 s101, v171, s49
.Lcmb_b1:
	s_add_u32 s50, s46, -1
	s_addc_u32 s51, s47, -1
	s_and_b64 vcc, s[50:51], s[46:47]
	s_mulk_i32 s43, 0x900
	s_ashr_i32 s47, s48, 31
	s_add_u32 s46, s48, s43
	s_addc_u32 s47, s47, 0
	s_mulk_i32 s7, 0x900
	s_ashr_i32 s43, s1, 31
	v_lshl_add_u64 v[214:215], s[46:47], 0, v[160:161]
	s_add_u32 s46, s7, s1
	s_addc_u32 s47, 0, s43
	v_lshl_add_u64 v[222:223], s[46:47], 0, v[160:161]
	v_lshlrev_b64 v[214:215], 11, v[214:215]
	v_lshlrev_b64 v[222:223], 11, v[222:223]
	v_lshl_add_u64 v[214:215], v[138:139], 0, v[214:215]
	v_lshl_add_u64 v[222:223], v[138:139], 0, v[222:223]
	global_load_dwordx2 v[216:217], v[214:215], off nt
	global_load_dwordx2 v[218:219], v[214:215], off offset:512 nt
	global_load_dwordx2 v[220:221], v[214:215], off offset:1024 nt
	s_nop 0
	global_load_dwordx2 v[214:215], v[214:215], off offset:1536 nt
	s_nop 0
	global_load_dwordx2 v[224:225], v[222:223], off nt
	global_load_dwordx2 v[230:231], v[222:223], off offset:512 nt
	global_load_dwordx2 v[194:195], v[222:223], off offset:1024 nt
	s_nop 0
	global_load_dwordx2 v[222:223], v[222:223], off offset:1536 nt
	s_waitcnt vmcnt(15)
	v_lshlrev_b32_e32 v198, 16, v178
	v_and_b32_e32 v199, 0xffff0000, v178
	s_waitcnt vmcnt(11)
	v_lshlrev_b32_e32 v206, 16, v186
	v_and_b32_e32 v207, 0xffff0000, v186
	v_lshlrev_b32_e32 v186, 16, v187
	v_and_b32_e32 v187, 0xffff0000, v187
	s_waitcnt vmcnt(10)
	v_lshlrev_b32_e32 v208, 16, v188
	v_and_b32_e32 v209, 0xffff0000, v188
	v_lshlrev_b32_e32 v188, 16, v189
	v_and_b32_e32 v189, 0xffff0000, v189
	s_waitcnt vmcnt(9)
	v_lshlrev_b32_e32 v210, 16, v190
	v_and_b32_e32 v211, 0xffff0000, v190
	v_lshlrev_b32_e32 v190, 16, v191
	v_and_b32_e32 v191, 0xffff0000, v191
	s_waitcnt vmcnt(8)
	v_lshlrev_b32_e32 v212, 16, v184
	v_and_b32_e32 v213, 0xffff0000, v184
	v_lshlrev_b32_e32 v184, 16, v185
	v_and_b32_e32 v185, 0xffff0000, v185
	v_lshlrev_b32_e32 v178, 16, v179
	v_and_b32_e32 v179, 0xffff0000, v179
	v_lshlrev_b32_e32 v200, 16, v180
	v_and_b32_e32 v201, 0xffff0000, v180
	v_lshlrev_b32_e32 v180, 16, v181
	v_and_b32_e32 v181, 0xffff0000, v181
	v_lshlrev_b32_e32 v202, 16, v182
	v_and_b32_e32 v203, 0xffff0000, v182
	v_lshlrev_b32_e32 v182, 16, v183
	v_and_b32_e32 v183, 0xffff0000, v183
	v_lshlrev_b32_e32 v204, 16, v176
	v_and_b32_e32 v205, 0xffff0000, v176
	v_lshlrev_b32_e32 v176, 16, v177
	v_and_b32_e32 v177, 0xffff0000, v177
	v_pk_mul_f32 v[184:185], s[6:7], v[184:185] op_sel_hi:[0,1]
	v_pk_mul_f32 v[212:213], s[6:7], v[212:213] op_sel_hi:[0,1]
	v_pk_mul_f32 v[190:191], s[6:7], v[190:191] op_sel_hi:[0,1]
	v_pk_mul_f32 v[210:211], s[6:7], v[210:211] op_sel_hi:[0,1]
	v_pk_mul_f32 v[188:189], s[6:7], v[188:189] op_sel_hi:[0,1]
	v_pk_mul_f32 v[208:209], s[6:7], v[208:209] op_sel_hi:[0,1]
	v_pk_mul_f32 v[186:187], s[6:7], v[186:187] op_sel_hi:[0,1]
	v_pk_mul_f32 v[206:207], s[6:7], v[206:207] op_sel_hi:[0,1]
	v_pk_fma_f32 v[198:199], s[0:1], v[198:199], v[206:207] op_sel_hi:[0,1,1]
	v_pk_fma_f32 v[178:179], s[0:1], v[178:179], v[186:187] op_sel_hi:[0,1,1]
	v_pk_fma_f32 v[186:187], s[0:1], v[200:201], v[208:209] op_sel_hi:[0,1,1]
	v_pk_fma_f32 v[180:181], s[0:1], v[180:181], v[188:189] op_sel_hi:[0,1,1]
	v_pk_fma_f32 v[188:189], s[0:1], v[202:203], v[210:211] op_sel_hi:[0,1,1]
	v_pk_fma_f32 v[182:183], s[0:1], v[182:183], v[190:191] op_sel_hi:[0,1,1]
	v_pk_fma_f32 v[190:191], s[0:1], v[204:205], v[212:213] op_sel_hi:[0,1,1]
	v_pk_fma_f32 v[176:177], s[0:1], v[176:177], v[184:185] op_sel_hi:[0,1,1]
	v_pk_add_f32 v[150:151], v[150:151], v[176:177]
	v_pk_add_f32 v[144:145], v[144:145], v[190:191]
	v_pk_add_f32 v[152:153], v[152:153], v[182:183]
	v_pk_add_f32 v[146:147], v[146:147], v[188:189]
	v_pk_add_f32 v[156:157], v[156:157], v[180:181]
	v_pk_add_f32 v[148:149], v[148:149], v[186:187]
	v_pk_add_f32 v[158:159], v[158:159], v[178:179]
	v_pk_add_f32 v[154:155], v[154:155], v[198:199]
	s_waitcnt vmcnt(7)
	v_lshlrev_b32_e32 v198, 16, v216
	v_and_b32_e32 v199, 0xffff0000, v216
	s_waitcnt vmcnt(3)
	v_lshlrev_b32_e32 v206, 16, v224
	v_and_b32_e32 v207, 0xffff0000, v224
	v_lshlrev_b32_e32 v224, 16, v225
	v_and_b32_e32 v225, 0xffff0000, v225
	s_waitcnt vmcnt(2)
	v_lshlrev_b32_e32 v208, 16, v230
	v_and_b32_e32 v209, 0xffff0000, v230
	v_lshlrev_b32_e32 v230, 16, v231
	v_and_b32_e32 v231, 0xffff0000, v231
	s_waitcnt vmcnt(1)
	v_lshlrev_b32_e32 v210, 16, v194
	v_and_b32_e32 v211, 0xffff0000, v194
	v_lshlrev_b32_e32 v194, 16, v195
	v_and_b32_e32 v195, 0xffff0000, v195
	s_waitcnt vmcnt(0)
	v_lshlrev_b32_e32 v212, 16, v222
	v_and_b32_e32 v213, 0xffff0000, v222
	v_lshlrev_b32_e32 v222, 16, v223
	v_and_b32_e32 v223, 0xffff0000, v223
	v_lshlrev_b32_e32 v216, 16, v217
	v_and_b32_e32 v217, 0xffff0000, v217
	v_lshlrev_b32_e32 v200, 16, v218
	v_and_b32_e32 v201, 0xffff0000, v218
	v_lshlrev_b32_e32 v218, 16, v219
	v_and_b32_e32 v219, 0xffff0000, v219
	v_lshlrev_b32_e32 v202, 16, v220
	v_and_b32_e32 v203, 0xffff0000, v220
	v_lshlrev_b32_e32 v220, 16, v221
	v_and_b32_e32 v221, 0xffff0000, v221
	v_lshlrev_b32_e32 v204, 16, v214
	v_and_b32_e32 v205, 0xffff0000, v214
	v_lshlrev_b32_e32 v214, 16, v215
	v_and_b32_e32 v215, 0xffff0000, v215
	v_pk_mul_f32 v[222:223], s[100:101], v[222:223] op_sel:[1,0] op_sel_hi:[1,1]
	v_pk_mul_f32 v[212:213], s[100:101], v[212:213] op_sel:[1,0] op_sel_hi:[1,1]
	v_pk_mul_f32 v[194:195], s[100:101], v[194:195] op_sel:[1,0] op_sel_hi:[1,1]
	v_pk_mul_f32 v[210:211], s[100:101], v[210:211] op_sel:[1,0] op_sel_hi:[1,1]
	v_pk_mul_f32 v[230:231], s[100:101], v[230:231] op_sel:[1,0] op_sel_hi:[1,1]
	v_pk_mul_f32 v[208:209], s[100:101], v[208:209] op_sel:[1,0] op_sel_hi:[1,1]
	v_pk_mul_f32 v[224:225], s[100:101], v[224:225] op_sel:[1,0] op_sel_hi:[1,1]
	v_pk_mul_f32 v[206:207], s[100:101], v[206:207] op_sel:[1,0] op_sel_hi:[1,1]
	v_pk_fma_f32 v[198:199], s[100:101], v[198:199], v[206:207] op_sel_hi:[0,1,1]
	v_pk_fma_f32 v[216:217], s[100:101], v[216:217], v[224:225] op_sel_hi:[0,1,1]
	v_pk_fma_f32 v[224:225], s[100:101], v[200:201], v[208:209] op_sel_hi:[0,1,1]
	v_pk_fma_f32 v[218:219], s[100:101], v[218:219], v[230:231] op_sel_hi:[0,1,1]
	v_pk_fma_f32 v[230:231], s[100:101], v[202:203], v[210:211] op_sel_hi:[0,1,1]
	v_pk_fma_f32 v[220:221], s[100:101], v[220:221], v[194:195] op_sel_hi:[0,1,1]
	v_pk_fma_f32 v[194:195], s[100:101], v[204:205], v[212:213] op_sel_hi:[0,1,1]
	v_pk_fma_f32 v[214:215], s[100:101], v[214:215], v[222:223] op_sel_hi:[0,1,1]
	v_pk_add_f32 v[150:151], v[150:151], v[214:215]
	v_pk_add_f32 v[144:145], v[144:145], v[194:195]
	v_pk_add_f32 v[152:153], v[152:153], v[220:221]
	v_pk_add_f32 v[146:147], v[146:147], v[230:231]
	v_pk_add_f32 v[156:157], v[156:157], v[218:219]
	v_pk_add_f32 v[148:149], v[148:149], v[224:225]
	v_pk_add_f32 v[158:159], v[158:159], v[216:217]
	v_pk_add_f32 v[154:155], v[154:155], v[198:199]
	v_mov_b64_e32 v[194:195], 0x100
	s_cmp_eq_u64 vcc, 0
	s_cbranch_scc1 .LBB0_137
	s_branch .LBB0_158
.Lcmb_noB:
	s_waitcnt vmcnt(7)
	v_lshlrev_b32_e32 v198, 16, v178
	v_and_b32_e32 v199, 0xffff0000, v178
	s_waitcnt vmcnt(3)
	v_lshlrev_b32_e32 v206, 16, v186
	v_and_b32_e32 v207, 0xffff0000, v186
	v_lshlrev_b32_e32 v186, 16, v187
	v_and_b32_e32 v187, 0xffff0000, v187
	s_waitcnt vmcnt(2)
	v_lshlrev_b32_e32 v208, 16, v188
	v_and_b32_e32 v209, 0xffff0000, v188
	v_lshlrev_b32_e32 v188, 16, v189
	v_and_b32_e32 v189, 0xffff0000, v189
	s_waitcnt vmcnt(1)
	v_lshlrev_b32_e32 v210, 16, v190
	v_and_b32_e32 v211, 0xffff0000, v190
	v_lshlrev_b32_e32 v190, 16, v191
	v_and_b32_e32 v191, 0xffff0000, v191
	s_waitcnt vmcnt(0)
	v_lshlrev_b32_e32 v212, 16, v184
	v_and_b32_e32 v213, 0xffff0000, v184
	v_lshlrev_b32_e32 v184, 16, v185
	v_and_b32_e32 v185, 0xffff0000, v185
	v_lshlrev_b32_e32 v178, 16, v179
	v_and_b32_e32 v179, 0xffff0000, v179
	v_lshlrev_b32_e32 v200, 16, v180
	v_and_b32_e32 v201, 0xffff0000, v180
	v_lshlrev_b32_e32 v180, 16, v181
	v_and_b32_e32 v181, 0xffff0000, v181
	v_lshlrev_b32_e32 v202, 16, v182
	v_and_b32_e32 v203, 0xffff0000, v182
	v_lshlrev_b32_e32 v182, 16, v183
	v_and_b32_e32 v183, 0xffff0000, v183
	v_lshlrev_b32_e32 v204, 16, v176
	v_and_b32_e32 v205, 0xffff0000, v176
	v_lshlrev_b32_e32 v176, 16, v177
	v_and_b32_e32 v177, 0xffff0000, v177
	v_pk_mul_f32 v[184:185], s[6:7], v[184:185] op_sel_hi:[0,1]
	v_pk_mul_f32 v[212:213], s[6:7], v[212:213] op_sel_hi:[0,1]
	v_pk_mul_f32 v[190:191], s[6:7], v[190:191] op_sel_hi:[0,1]
	v_pk_mul_f32 v[210:211], s[6:7], v[210:211] op_sel_hi:[0,1]
	v_pk_mul_f32 v[188:189], s[6:7], v[188:189] op_sel_hi:[0,1]
	v_pk_mul_f32 v[208:209], s[6:7], v[208:209] op_sel_hi:[0,1]
	v_pk_mul_f32 v[186:187], s[6:7], v[186:187] op_sel_hi:[0,1]
	v_pk_mul_f32 v[206:207], s[6:7], v[206:207] op_sel_hi:[0,1]
	v_pk_fma_f32 v[198:199], s[0:1], v[198:199], v[206:207] op_sel_hi:[0,1,1]
	v_pk_fma_f32 v[178:179], s[0:1], v[178:179], v[186:187] op_sel_hi:[0,1,1]
	v_pk_fma_f32 v[186:187], s[0:1], v[200:201], v[208:209] op_sel_hi:[0,1,1]
	v_pk_fma_f32 v[180:181], s[0:1], v[180:181], v[188:189] op_sel_hi:[0,1,1]
	v_pk_fma_f32 v[188:189], s[0:1], v[202:203], v[210:211] op_sel_hi:[0,1,1]
	v_pk_fma_f32 v[182:183], s[0:1], v[182:183], v[190:191] op_sel_hi:[0,1,1]
	v_pk_fma_f32 v[190:191], s[0:1], v[204:205], v[212:213] op_sel_hi:[0,1,1]
	v_pk_fma_f32 v[176:177], s[0:1], v[176:177], v[184:185] op_sel_hi:[0,1,1]
	v_pk_add_f32 v[150:151], v[150:151], v[176:177]
	v_pk_add_f32 v[144:145], v[144:145], v[190:191]
	v_pk_add_f32 v[152:153], v[152:153], v[182:183]
	v_pk_add_f32 v[146:147], v[146:147], v[188:189]
	v_pk_add_f32 v[156:157], v[156:157], v[180:181]
	v_pk_add_f32 v[148:149], v[148:149], v[186:187]
	v_pk_add_f32 v[158:159], v[158:159], v[178:179]
	v_pk_add_f32 v[154:155], v[154:155], v[198:199]
	s_branch .LBB0_137
